# P11 unit traversal per XCD: 2 row tiles x 16 column tiles per round (weights + round's activation panels resident in the Infinity Cache) instead of 8 x 4
# baseline (speedup 1.0000x reference)
; #define PG8_STAGE(bufoff, gbase, voff) do { const char* _gb = (const char*)(gbase); asm volatile("" : "+s"(_gb)); _Pragma("unroll") for (int _i = 0; _i < 2; ++_i) \
;         __builtin_amdgcn_global_load_lds((const unsigned*)(_gb + (voff)[_i]), (PG8_LAS unsigned*)(lds + (bufoff) + ldsw + _i * 8192), 16, 0, 0); } while (0)
; #define PG8_WAIT_V(n) asm volatile("s_waitcnt vmcnt(" #n ")" ::: "memory")
; #define PG8_BAR __builtin_amdgcn_s_barrier()
;     __host__ __device__ bool next(int i, Unit& u) const {
;         u.half = 0;
;         long L = (long)i * G + c;
;         if (tail > 0) { if (i > 0) return false; const int nt = nwg - tail * G; if (nt <= 0 || 2 * nt > G || c >= 2 * nt) return false; L = (long)tail * G + (c % nt); u.half = 1 + c / nt; }
;         else if (i >= rmax) return false;
;         if (L >= nwg) return false;
;         int wgid = (int)L; { const int q = nwg / NXCD, r = nwg % NXCD, xcd = wgid % NXCD, off = wgid / NXCD; wgid = (xcd < r ? xcd * (q + 1) : r * (q + 1) + (xcd - r) * q) + off; }
;         const int nig = wgm * nN, gid = wgid / nig, fm = gid * wgm, gsz = (nM - fm) < wgm ? (nM - fm) : wgm;
;         u.pm = pm0 + fm + ((wgid % nig) % gsz); u.pn = (wgid % nig) / gsz; return true;
; template <class Epi, class Sched, bool ALIGN_EPI = false, bool SP2 = false, bool HALFM = false>
; __device__ __forceinline__ void gemm_phase(PG8_LAS unsigned char* lds, const Gemm g, const Sched& S, const Epi& E) {
;     ...
;     bf16x8 At[4][2], B0[2][2], B1[2][2];
;     const char* cA = (const char*)g.A + (size_t)cur.pm * tstepA + ((HALFM && cur.half == 2) ? 16384 : 0); const char* cB = (const char*)g.Bt + (size_t)cur.pn * tstep;
;     S.a_ready(cur);
;     if constexpr (SP2) {
;         PG8_STAGE(PG8_SB(0, 0), cB, voffB); PG8_STAGE(PG8_SB(0, 1), cB + hstep, voffB); PG8_STAGE(PG8_SA(0, 0), cA, voffA); PG8_STAGE(PG8_SA(0, 1), cA + hstepA, voffA);
;         if (wr == 1) PG8_BAR;
;         PG8_WAIT_V(2); PG8_BAR;
;         PG8_STAGE(PG8_SB(1, 0), cB + kstep, voffB); PG8_STAGE(PG8_SA(1, 0), cA + kstep, voffA); PG8_STAGE(PG8_SB(1, 1), cB + hstep + kstep, voffB);
;         PG8_WAIT_V(6); PG8_BAR;
;         PG8_STAGE(PG8_SA(1, 1), cA + kstep + hstepA, voffA);
.LBB0_1405:
	s_lshr_b32 s7, s8, 6
	s_lshr_b32 s9, s8, 8
	s_lshl_b32 s20, s7, 10
	s_add_u32 s21, s84, 0x33600000
	s_addc_u32 s22, s85, 0
	s_add_u32 s23, s84, 0x10800000
	s_addc_u32 s24, s85, 0
	s_add_i32 s0, s4, s0
	s_ashr_i32 s1, s0, 31
	s_lshr_b32 s1, s1, 25
	s_add_i32 s1, s0, s1
	s_ashr_i32 s4, s1, 7
	s_and_b32 s1, s1, 0xff80
	s_sub_i32 s0, s0, s1
	s_bfe_i32 s1, s0, 0x80000
	s_bfe_u32 s1, s1, 0x3000c
	s_add_i32 s1, s0, s1
	s_bfe_i32 s5, s1, 0x80000
	s_and_b32 s1, s1, 0xf8
	s_sub_i32 s0, s0, s1
	s_lshl_b32 s4, s4, 3
	s_sext_i32_i16 s5, s5
	s_sext_i32_i8 s0, s0
	s_add_i32 s48, s4, s0
	s_and_b32 s0, s2, 7
	s_lshl_b32 s0, s0, 3
	s_bfe_u32 s1, s2, 0x10003
	s_add_i32 s0, s0, s1
	s_lshr_b32 s1, s2, 4
	s_lshl_b32 s1, s1, 3
	s_cmp_eq_u32 s80, 0x100
	s_cselect_b32 s48, s0, s48
	s_cselect_b32 s5, s1, s5
	s_ashr_i32 s0, s5, 3
	s_lshr_b32 s6, s5, 3
	s_mul_hi_i32 s1, s0, 0x560000
	s_mul_i32 s0, s0, 0x560000
	s_add_u32 s14, s23, s0
	s_addc_u32 s15, s24, s1
	s_mov_b64 s[0:1], s[14:15]
	s_add_i32 s25, s20, 0
	v_lshlrev_b32_e32 v128, 4, v0
	s_add_i32 m0, s25, 0x10000
	v_mov_b32_e32 v129, 0
	v_lshl_add_u64 v[2:3], s[0:1], 0, v[128:129]
	global_load_lds_dwordx4 v128, s[0:1]
	s_mov_b64 s[0:1], 0x2000
	s_add_i32 m0, s25, 0x12000
	v_lshl_add_u64 v[2:3], v[2:3], 0, s[0:1]
	s_add_u32 s4, s14, 0x4000
	global_load_lds_dwordx4 v[2:3], off
	s_addc_u32 s5, s15, 0
	s_add_i32 m0, s25, 0x14000
	s_mul_i32 s11, s48, 0x560000
	s_mul_hi_i32 s10, s48, 0x560000
	global_load_lds_dwordx4 v128, s[4:5]
	s_add_i32 m0, s25, 0x16000
	s_add_u32 s16, s21, s11
	v_lshl_add_u64 v[2:3], s[4:5], 0, v[128:129]
	s_addc_u32 s17, s22, s10
	v_lshl_add_u64 v[2:3], v[2:3], 0, s[0:1]
	s_mov_b64 s[4:5], s[16:17]
	global_load_lds_dwordx4 v[2:3], off
	s_mov_b32 m0, s25
	s_add_i32 s26, s25, 0x2000
	v_lshl_add_u64 v[2:3], s[4:5], 0, v[128:129]
	global_load_lds_dwordx4 v128, s[4:5]
	s_add_u32 s4, s16, 0x4000
	v_lshl_add_u64 v[2:3], v[2:3], 0, s[0:1]
	s_mov_b32 m0, s26
	s_addc_u32 s5, s17, 0
	s_add_i32 s27, s25, 0x4000
	global_load_lds_dwordx4 v[2:3], off
	s_mov_b32 m0, s27
	v_lshl_add_u64 v[2:3], s[4:5], 0, v[128:129]
	s_add_i32 s28, s25, 0x6000
	global_load_lds_dwordx4 v128, s[4:5]
	v_lshl_add_u64 v[2:3], v[2:3], 0, s[0:1]
	s_mov_b32 m0, s28
	s_cmp_eq_u32 s9, 1
	global_load_lds_dwordx4 v[2:3], off
	s_cselect_b64 s[4:5], -1, 0
	s_cmp_lg_u32 s9, 1
	s_mov_b32 s12, 0
	s_cbranch_scc1 .LBB0_1407
	s_barrier

;     __host__ __device__ bool next(int i, Unit& u) const {
;     ...
;         if (tail > 0) { if (i > 0) return false; const int nt = nwg - tail * G; if (nt <= 0 || 2 * nt > G || c >= 2 * nt) return false; L = (long)tail * G + (c % nt); u.half = 1 + c / nt; }
;         else if (i >= rmax) return false;
;         if (L >= nwg) return false;
;         int wgid = (int)L; { const int q = nwg / NXCD, r = nwg % NXCD, xcd = wgid % NXCD, off = wgid / NXCD; wgid = (xcd < r ? xcd * (q + 1) : r * (q + 1) + (xcd - r) * q) + off; }
;         const int nig = wgm * nN, gid = wgid / nig, fm = gid * wgm, gsz = (nM - fm) < wgm ? (nM - fm) : wgm;
;         u.pm = pm0 + fm + ((wgid % nig) % gsz); u.pn = (wgid % nig) / gsz; return true;
; template <class Epi, class Sched, bool ALIGN_EPI = false, bool SP2 = false, bool HALFM = false>
; __device__ __forceinline__ void gemm_phase(PG8_LAS unsigned char* lds, const Gemm g, const Sched& S, const Epi& E) {
;     ...
;         const bool has_next = S.next(ui + 1, nxt);
;         const char* nA = has_next ? (const char*)g.A + (size_t)nxt.pm * tstepA + ((HALFM && nxt.half == 2) ? 16384 : 0) : cA; const char* nB = has_next ? (const char*)g.Bt + (size_t)nxt.pn * tstep : cB;
.LBB0_1416:
	s_ashr_i32 s0, s8, 3
	s_add_i32 s0, s10, s0
	s_ashr_i32 s1, s0, 31
	s_lshr_b32 s1, s1, 25
	s_add_i32 s1, s0, s1
	s_ashr_i32 s8, s1, 7
	s_lshl_b32 s8, s8, 3
	s_sub_i32 s9, 64, s8
	s_min_i32 s9, s9, 8
	s_abs_i32 s10, s9
	v_cvt_f32_u32_e32 v0, s10
	s_sub_i32 s13, 0, s10
	s_and_b32 s1, s1, 0xffffff80
	s_sub_i32 s0, s0, s1
	v_rcp_iflag_f32_e32 v0, v0
	s_abs_i32 s1, s0
	s_xor_b32 s11, s0, s9
	s_ashr_i32 s11, s11, 31
	v_mul_f32_e32 v0, 0x4f7ffffe, v0
	v_cvt_u32_f32_e32 v0, v0
	s_nop 0
	v_readfirstlane_b32 s18, v0
	s_mul_i32 s13, s13, s18
	s_mul_hi_u32 s13, s18, s13
	s_add_i32 s18, s18, s13
	s_mul_hi_u32 s13, s1, s18
	s_mul_i32 s18, s13, s10
	s_sub_i32 s1, s1, s18
	s_add_i32 s19, s13, 1
	s_sub_i32 s18, s1, s10
	s_cmp_ge_u32 s1, s10
	s_cselect_b32 s13, s19, s13
	s_cselect_b32 s1, s18, s1
	s_add_i32 s18, s13, 1
	s_cmp_ge_u32 s1, s10
	s_cselect_b32 s1, s18, s13
	s_xor_b32 s1, s1, s11
	s_sub_i32 s46, s1, s11
	s_mul_i32 s1, s46, s9
	s_sub_i32 s0, s0, s1
	s_add_i32 s47, s8, s0
	s_and_b32 s0, s2, 7
	s_lshl_b32 s0, s0, 3
	s_bfe_u32 s1, s2, 0x10003
	s_add_i32 s0, s0, s1
	s_lshl_b32 s1, s45, 1
	s_add_i32 s0, s0, s1
	s_lshr_b32 s1, s2, 4
	s_cmp_eq_u32 s80, 0x100
	s_cselect_b32 s47, s0, s47
	s_cselect_b32 s46, s1, s46
	s_mov_b64 s[8:9], -1
